# v24 + static s_setprio 1 for the younger wave half (waves 4-7) at the entry of the attention, retention and router phases
# speedup vs baseline: 1.0000x; 1.0000x over previous
.LBB0_677:
	s_cmp_lt_u32 s88, 4
	s_cbranch_scc1 .Lprio_y0
	s_setprio 1
